# baseline (speedup 1.0000x reference)
.Lrec_try0:
	s_cmp_eq_u32 s45, 0
	s_cbranch_scc1 .Lrec_tm
	s_bitcmp1_b32 s45, 0
	s_cbranch_scc1 .Lrec_stall
	v_mfma_f32_16x16x32_f16 v[198:201], v[152:155], v[16:19], 0
	v_mfma_f32_16x16x32_f16 v[202:205], v[48:51], v[16:19], 0
	v_mfma_f32_16x16x32_f16 v[212:215], v[88:91], v[16:19], 0
	v_mfma_f32_16x16x32_f16 v[216:219], v[92:95], v[16:19], 0
	v_mfma_f32_16x16x32_f16 v[220:223], v[108:111], v[16:19], 0
	v_mfma_f32_16x16x32_f16 v[224:227], v[112:115], v[16:19], 0
	v_mfma_f32_16x16x32_f16 v[228:231], v[140:143], v[16:19], 0
	v_mfma_f32_16x16x32_f16 v[232:235], v[32:35], v[16:19], v[160:163]
	s_mov_b32 s46, 1

.Lrec_tm:
	v_mfma_f32_16x16x32_f16 v[198:201], v[152:155], v[16:19], 0
	v_mfma_f32_16x16x32_f16 v[198:201], v[52:55], v[20:23], v[198:201]
	v_mfma_f32_16x16x32_f16 v[198:201], v[60:63], v[24:27], v[198:201]
	v_mfma_f32_16x16x32_f16 v[198:201], v[72:75], v[28:31], v[198:201]
	v_mfma_f32_16x16x32_f16 v[202:205], v[48:51], v[16:19], 0
	v_mfma_f32_16x16x32_f16 v[202:205], v[56:59], v[20:23], v[202:205]
	v_mfma_f32_16x16x32_f16 v[202:205], v[64:67], v[24:27], v[202:205]
	v_mfma_f32_16x16x32_f16 v[202:205], v[68:71], v[28:31], v[202:205]
	v_mfma_f32_16x16x32_f16 v[212:215], v[88:91], v[16:19], 0
	v_mfma_f32_16x16x32_f16 v[212:215], v[76:79], v[20:23], v[212:215]
	v_mfma_f32_16x16x32_f16 v[212:215], v[80:83], v[24:27], v[212:215]
	v_mfma_f32_16x16x32_f16 v[212:215], v[84:87], v[28:31], v[212:215]
	v_add_u32_e32 v197, v173, v188
	ds_write_b128 v197, v[198:201] offset:1024
	v_mfma_f32_16x16x32_f16 v[216:219], v[92:95], v[16:19], 0
	v_mfma_f32_16x16x32_f16 v[216:219], v[96:99], v[20:23], v[216:219]
	v_mfma_f32_16x16x32_f16 v[216:219], v[100:103], v[24:27], v[216:219]
	v_mfma_f32_16x16x32_f16 v[216:219], v[104:107], v[28:31], v[216:219]
	v_add_u32_e32 v197, v173, v189
	ds_write_b128 v197, v[202:205] offset:2048
	v_mfma_f32_16x16x32_f16 v[220:223], v[108:111], v[16:19], 0
	v_mfma_f32_16x16x32_f16 v[220:223], v[116:119], v[20:23], v[220:223]
	v_mfma_f32_16x16x32_f16 v[220:223], v[124:127], v[24:27], v[220:223]
	v_mfma_f32_16x16x32_f16 v[220:223], v[136:139], v[28:31], v[220:223]
	v_add_u32_e32 v197, v173, v190
	ds_write_b128 v197, v[212:215] offset:3072
	v_mfma_f32_16x16x32_f16 v[224:227], v[112:115], v[16:19], 0
	v_mfma_f32_16x16x32_f16 v[224:227], v[120:123], v[20:23], v[224:227]
	v_mfma_f32_16x16x32_f16 v[224:227], v[128:131], v[24:27], v[224:227]
	v_mfma_f32_16x16x32_f16 v[224:227], v[132:135], v[28:31], v[224:227]
	v_add_u32_e32 v197, v173, v194
	ds_write_b128 v197, v[216:219] offset:4096
	v_mfma_f32_16x16x32_f16 v[228:231], v[140:143], v[16:19], 0
	v_mfma_f32_16x16x32_f16 v[228:231], v[144:147], v[20:23], v[228:231]
	v_mfma_f32_16x16x32_f16 v[228:231], v[148:151], v[24:27], v[228:231]
	v_mfma_f32_16x16x32_f16 v[228:231], v[156:159], v[28:31], v[228:231]
	v_add_u32_e32 v197, v173, v191
	ds_write_b128 v197, v[220:223] offset:5120
	v_mfma_f32_16x16x32_f16 v[232:235], v[32:35], v[16:19], v[160:163]
	v_mfma_f32_16x16x32_f16 v[232:235], v[36:39], v[20:23], v[232:235]
	v_mfma_f32_16x16x32_f16 v[232:235], v[40:43], v[24:27], v[232:235]
	v_mfma_f32_16x16x32_f16 v[232:235], v[44:47], v[28:31], v[232:235]
	v_add_u32_e32 v197, v173, v192
	ds_write_b128 v197, v[224:227] offset:6144
	v_add_u32_e32 v197, v173, v193
	ds_write_b128 v197, v[228:231] offset:7168
	s_mov_b32 s55, 1
